# gather counted waits: u-section loops allow 10 rows in flight (vmcnt 9) while v-section stays at 7
# speedup vs baseline: 1.0040x; 1.0040x over previous
.LBB0_1419:
	v_mov_b32_e32 v69, v1
	v_mov_b32_e32 v83, v1
	s_waitcnt vmcnt(9)
	v_dot8c_i32_i4_e32 v69, v6, v74
	v_dot8c_i32_i4_e32 v83, v6, v70
	v_dot8c_i32_i4_e32 v69, v7, v75
	v_dot8c_i32_i4_e32 v83, v7, v71
	s_add_i32 s62, s57, -15
	v_dot8c_i32_i4_e32 v69, v8, v76
	v_dot8c_i32_i4_e32 v83, v8, v72
	s_cmp_lt_u32 s56, 3
	v_dot8c_i32_i4_e32 v69, v9, v77
	v_dot8c_i32_i4_e32 v83, v9, v73
	s_cselect_b64 vcc, -1, 0
	s_nop 1
	v_lshl_add_u32 v6, v69, 4, v83
	v_cndmask_b32_e32 v83, v79, v78, vcc
	v_cvt_f32_i32_e32 v69, v6
	v_readlane_b32 s62, v83, s62
	s_lshl_b32 s62, s62, 10
	s_nop 3
	buffer_load_dwordx4 v[6:9], v0, s[92:95], s62 offen
	v_mov_b32_e32 v84, v1
	v_mov_b32_e32 v85, v1
	s_waitcnt vmcnt(9)
	v_dot8c_i32_i4_e32 v84, v14, v74
	v_dot8c_i32_i4_e32 v85, v14, v70
	v_dot8c_i32_i4_e32 v84, v15, v75
	v_dot8c_i32_i4_e32 v85, v15, v71
	v_dot8c_i32_i4_e32 v84, v16, v76
	v_dot8c_i32_i4_e32 v85, v16, v72
	s_add_i32 s62, s57, -14
	v_dot8c_i32_i4_e32 v84, v17, v77
	v_dot8c_i32_i4_e32 v85, v17, v73
	v_readlane_b32 s62, v83, s62
	s_lshl_b32 s62, s62, 10
	s_nop 0
	v_lshl_add_u32 v14, v84, 4, v85
	v_cvt_f32_i32_e32 v84, v14
	s_nop 0
	buffer_load_dwordx4 v[14:17], v0, s[92:95], s62 offen
	v_mov_b32_e32 v85, v1
	v_mov_b32_e32 v86, v1
	s_waitcnt vmcnt(9)
	v_dot8c_i32_i4_e32 v85, v30, v74
	v_dot8c_i32_i4_e32 v86, v30, v70
	v_dot8c_i32_i4_e32 v85, v31, v75
	v_dot8c_i32_i4_e32 v86, v31, v71
	v_dot8c_i32_i4_e32 v85, v32, v76
	v_dot8c_i32_i4_e32 v86, v32, v72
	s_add_i32 s62, s57, -13
	v_dot8c_i32_i4_e32 v85, v33, v77
	v_dot8c_i32_i4_e32 v86, v33, v73
	v_readlane_b32 s62, v83, s62
	s_lshl_b32 s62, s62, 10
	s_nop 0
	v_lshl_add_u32 v30, v85, 4, v86
	v_cvt_f32_i32_e32 v85, v30
	s_nop 0
	buffer_load_dwordx4 v[30:33], v0, s[92:95], s62 offen
	v_mov_b32_e32 v86, v1
	v_mov_b32_e32 v87, v1
	s_waitcnt vmcnt(9)
	v_dot8c_i32_i4_e32 v86, v46, v74
	v_dot8c_i32_i4_e32 v87, v46, v70
	v_dot8c_i32_i4_e32 v86, v47, v75
	v_dot8c_i32_i4_e32 v87, v47, v71
	v_dot8c_i32_i4_e32 v86, v48, v76
	v_dot8c_i32_i4_e32 v87, v48, v72
	s_add_i32 s62, s57, -12
	v_dot8c_i32_i4_e32 v86, v49, v77
	v_dot8c_i32_i4_e32 v87, v49, v73
	v_readlane_b32 s62, v83, s62
	s_lshl_b32 s62, s62, 10
	s_nop 0
	v_lshl_add_u32 v46, v86, 4, v87
	v_cvt_f32_i32_e32 v86, v46
	s_nop 0
	buffer_load_dwordx4 v[46:49], v0, s[92:95], s62 offen
	v_mov_b32_e32 v87, v1
	v_mov_b32_e32 v88, v1
	s_waitcnt vmcnt(9)
	v_dot8c_i32_i4_e32 v87, v2, v74
	v_dot8c_i32_i4_e32 v88, v2, v70
	v_dot8c_i32_i4_e32 v87, v3, v75
	v_dot8c_i32_i4_e32 v88, v3, v71
	v_dot8c_i32_i4_e32 v87, v4, v76
	v_dot8c_i32_i4_e32 v88, v4, v72
	s_add_i32 s62, s57, -11
	v_dot8c_i32_i4_e32 v87, v5, v77
	v_dot8c_i32_i4_e32 v88, v5, v73
	v_readlane_b32 s62, v83, s62
	s_lshl_b32 s62, s62, 10
	s_nop 0
	v_lshl_add_u32 v2, v87, 4, v88
	v_cvt_f32_i32_e32 v87, v2
	s_nop 0
	buffer_load_dwordx4 v[2:5], v0, s[92:95], s62 offen
	v_mov_b32_e32 v88, v1
	v_mov_b32_e32 v89, v1
	s_waitcnt vmcnt(9)
	v_dot8c_i32_i4_e32 v88, v22, v74
	v_dot8c_i32_i4_e32 v89, v22, v70
	v_dot8c_i32_i4_e32 v88, v23, v75
	v_dot8c_i32_i4_e32 v89, v23, v71
	v_dot8c_i32_i4_e32 v88, v24, v76
	v_dot8c_i32_i4_e32 v89, v24, v72
	s_add_i32 s62, s57, -10
	v_dot8c_i32_i4_e32 v88, v25, v77
	v_dot8c_i32_i4_e32 v89, v25, v73
	v_readlane_b32 s62, v83, s62
	s_lshl_b32 s62, s62, 10
	s_nop 0
	v_lshl_add_u32 v22, v88, 4, v89
	v_cvt_f32_i32_e32 v88, v22
	s_nop 0
	buffer_load_dwordx4 v[22:25], v0, s[92:95], s62 offen
	v_mov_b32_e32 v89, v1
	v_mov_b32_e32 v90, v1
	s_waitcnt vmcnt(9)
	v_dot8c_i32_i4_e32 v89, v38, v74
	v_dot8c_i32_i4_e32 v90, v38, v70
	v_dot8c_i32_i4_e32 v89, v39, v75
	v_dot8c_i32_i4_e32 v90, v39, v71
	v_dot8c_i32_i4_e32 v89, v40, v76
	v_dot8c_i32_i4_e32 v90, v40, v72
	s_add_i32 s62, s57, -9
	v_dot8c_i32_i4_e32 v89, v41, v77
	v_dot8c_i32_i4_e32 v90, v41, v73
	v_readlane_b32 s62, v83, s62
	s_lshl_b32 s62, s62, 10
	s_nop 0
	v_lshl_add_u32 v38, v89, 4, v90
	v_cvt_f32_i32_e32 v89, v38
	s_nop 0
	buffer_load_dwordx4 v[38:41], v0, s[92:95], s62 offen
	v_mov_b32_e32 v90, v1
	v_mov_b32_e32 v91, v1
	s_waitcnt vmcnt(9)
	v_dot8c_i32_i4_e32 v90, v54, v74
	v_dot8c_i32_i4_e32 v91, v54, v70
	v_dot8c_i32_i4_e32 v90, v55, v75
	v_dot8c_i32_i4_e32 v91, v55, v71
	v_dot8c_i32_i4_e32 v90, v56, v76
	v_dot8c_i32_i4_e32 v91, v56, v72
	s_add_i32 s62, s57, -8
	v_dot8c_i32_i4_e32 v90, v57, v77
	v_dot8c_i32_i4_e32 v91, v57, v73
	v_readlane_b32 s62, v83, s62
	s_lshl_b32 s62, s62, 10
	s_nop 0
	v_lshl_add_u32 v54, v90, 4, v91
	v_cvt_f32_i32_e32 v90, v54
	s_nop 0
	buffer_load_dwordx4 v[54:57], v0, s[92:95], s62 offen
	v_mov_b32_e32 v91, v1
	v_mov_b32_e32 v92, v1
	s_waitcnt vmcnt(9)
	v_dot8c_i32_i4_e32 v91, v10, v74
	v_dot8c_i32_i4_e32 v92, v10, v70
	v_dot8c_i32_i4_e32 v91, v11, v75
	v_dot8c_i32_i4_e32 v92, v11, v71
	v_dot8c_i32_i4_e32 v91, v12, v76
	v_dot8c_i32_i4_e32 v92, v12, v72
	s_add_i32 s62, s57, -7
	v_dot8c_i32_i4_e32 v91, v13, v77
	v_dot8c_i32_i4_e32 v92, v13, v73
	v_readlane_b32 s62, v83, s62
	s_lshl_b32 s62, s62, 10
	s_nop 0
	v_lshl_add_u32 v10, v91, 4, v92
	v_cvt_f32_i32_e32 v91, v10
	s_nop 0
	buffer_load_dwordx4 v[10:13], v0, s[92:95], s62 offen
	v_mov_b32_e32 v92, v1
	v_mov_b32_e32 v93, v1
	s_waitcnt vmcnt(9)
	v_dot8c_i32_i4_e32 v92, v26, v74
	v_dot8c_i32_i4_e32 v93, v26, v70
	v_dot8c_i32_i4_e32 v92, v27, v75
	v_dot8c_i32_i4_e32 v93, v27, v71
	v_dot8c_i32_i4_e32 v92, v28, v76
	v_dot8c_i32_i4_e32 v93, v28, v72
	s_add_i32 s62, s57, -6
	v_dot8c_i32_i4_e32 v92, v29, v77
	v_dot8c_i32_i4_e32 v93, v29, v73
	v_readlane_b32 s62, v83, s62
	s_lshl_b32 s62, s62, 10
	s_nop 0
	v_lshl_add_u32 v26, v92, 4, v93
	v_cvt_f32_i32_e32 v92, v26
	s_nop 0
	buffer_load_dwordx4 v[26:29], v0, s[92:95], s62 offen
	v_mov_b32_e32 v93, v1
	v_mov_b32_e32 v94, v1
	s_waitcnt vmcnt(9)
; __device__ __forceinline__ float gelu_as(float v) {
;     const float av = fabsf(v), t = __builtin_amdgcn_rcpf(av * 0.2316418882f + 1.0f);
;     float q = t * 0.5307027145f + (-0.7265760135f); q = q * t + 0.7107068705f; q = q * t + (-0.142248368f); q = q * t + 0.127414796f; q = q * t;
;     const float m = v * (q * __builtin_amdgcn_exp2f((v * v) * (-0.72134752044f)));
;     return v < 0.f ? m : v - m;
; }
	v_dot8c_i32_i4_e32 v93, v42, v74
	v_dot8c_i32_i4_e32 v94, v42, v70
	v_dot8c_i32_i4_e32 v93, v43, v75
	v_dot8c_i32_i4_e32 v94, v43, v71
	v_dot8c_i32_i4_e32 v93, v44, v76
	v_dot8c_i32_i4_e32 v94, v44, v72
	s_add_i32 s62, s57, -5
	v_dot8c_i32_i4_e32 v93, v45, v77
	v_dot8c_i32_i4_e32 v94, v45, v73
	v_readlane_b32 s62, v83, s62
	s_lshl_b32 s62, s62, 10
	s_nop 0
	v_lshl_add_u32 v42, v93, 4, v94
	v_cvt_f32_i32_e32 v93, v42
	s_nop 0
	buffer_load_dwordx4 v[42:45], v0, s[92:95], s62 offen
	v_mov_b32_e32 v94, v1
	v_mov_b32_e32 v95, v1
	s_waitcnt vmcnt(9)
	v_dot8c_i32_i4_e32 v94, v58, v74
	v_dot8c_i32_i4_e32 v95, v58, v70
	v_dot8c_i32_i4_e32 v94, v59, v75
	v_dot8c_i32_i4_e32 v95, v59, v71
	v_dot8c_i32_i4_e32 v94, v60, v76
	v_dot8c_i32_i4_e32 v95, v60, v72
	s_add_i32 s62, s57, -4
	v_dot8c_i32_i4_e32 v94, v61, v77
	v_dot8c_i32_i4_e32 v95, v61, v73
	v_readlane_b32 s62, v83, s62
	s_lshl_b32 s62, s62, 10
	s_nop 0
	v_lshl_add_u32 v58, v94, 4, v95
	v_cvt_f32_i32_e32 v94, v58
	s_nop 0
	buffer_load_dwordx4 v[58:61], v0, s[92:95], s62 offen
	v_mov_b32_e32 v95, v1
	v_mov_b32_e32 v96, v1
	s_waitcnt vmcnt(9)
	v_dot8c_i32_i4_e32 v95, v18, v74
	v_dot8c_i32_i4_e32 v96, v18, v70
	v_dot8c_i32_i4_e32 v95, v19, v75
	v_dot8c_i32_i4_e32 v96, v19, v71
	v_dot8c_i32_i4_e32 v95, v20, v76
	v_dot8c_i32_i4_e32 v96, v20, v72
	s_add_i32 s62, s57, -3
	v_dot8c_i32_i4_e32 v95, v21, v77
	v_dot8c_i32_i4_e32 v96, v21, v73
	v_readlane_b32 s62, v83, s62
	s_lshl_b32 s62, s62, 10
	s_nop 0
	v_lshl_add_u32 v18, v95, 4, v96
	v_cvt_f32_i32_e32 v95, v18
	s_nop 0
	buffer_load_dwordx4 v[18:21], v0, s[92:95], s62 offen
	v_mov_b32_e32 v96, v1
	v_mov_b32_e32 v97, v1
	s_waitcnt vmcnt(9)
	v_dot8c_i32_i4_e32 v96, v34, v74
	v_dot8c_i32_i4_e32 v97, v34, v70
	v_dot8c_i32_i4_e32 v96, v35, v75
	v_dot8c_i32_i4_e32 v97, v35, v71
	v_dot8c_i32_i4_e32 v96, v36, v76
	v_dot8c_i32_i4_e32 v97, v36, v72
	s_add_i32 s62, s57, -2
	v_dot8c_i32_i4_e32 v96, v37, v77
	v_dot8c_i32_i4_e32 v97, v37, v73
	v_readlane_b32 s62, v83, s62
	s_lshl_b32 s62, s62, 10
	s_nop 0
	v_lshl_add_u32 v34, v96, 4, v97
	v_cvt_f32_i32_e32 v96, v34
	s_nop 0
	buffer_load_dwordx4 v[34:37], v0, s[92:95], s62 offen
	v_mov_b32_e32 v97, v1
	v_mov_b32_e32 v98, v1
	s_waitcnt vmcnt(9)
	v_dot8c_i32_i4_e32 v97, v50, v74
	v_dot8c_i32_i4_e32 v98, v50, v70
	v_dot8c_i32_i4_e32 v97, v51, v75
	v_dot8c_i32_i4_e32 v98, v51, v71
	v_dot8c_i32_i4_e32 v97, v52, v76
	v_dot8c_i32_i4_e32 v98, v52, v72
	s_add_i32 s62, s57, -1
	v_dot8c_i32_i4_e32 v97, v53, v77
	v_dot8c_i32_i4_e32 v98, v53, v73
	v_readlane_b32 s62, v83, s62
	s_lshl_b32 s62, s62, 10
	s_nop 0
	v_lshl_add_u32 v50, v97, 4, v98
	v_cvt_f32_i32_e32 v97, v50
	s_nop 0
	buffer_load_dwordx4 v[50:53], v0, s[92:95], s62 offen
	v_mov_b32_e32 v98, v1
	v_mov_b32_e32 v99, v1
	s_waitcnt vmcnt(9)
	v_dot8c_i32_i4_e32 v98, v62, v74
	v_dot8c_i32_i4_e32 v99, v62, v70
	v_dot8c_i32_i4_e32 v98, v63, v75
	v_dot8c_i32_i4_e32 v99, v63, v71
	v_readlane_b32 s62, v83, s57
	v_dot8c_i32_i4_e32 v98, v64, v76
	v_dot8c_i32_i4_e32 v99, v64, v72
	s_lshl_b32 s62, s62, 10
	v_dot8c_i32_i4_e32 v98, v65, v77
	v_dot8c_i32_i4_e32 v99, v65, v73
	buffer_load_dwordx4 v[62:65], v0, s[92:95], s62 offen
	s_nop 1
	v_lshl_add_u32 v83, v98, 4, v99
	v_cvt_f32_i32_e32 v83, v83
	v_cndmask_b32_e64 v98, v91, v69, s[0:1]
	v_cndmask_b32_e64 v69, v69, v91, s[0:1]
	v_cndmask_b32_e64 v91, v92, v84, s[0:1]
	v_cndmask_b32_e64 v84, v84, v92, s[0:1]
	v_cndmask_b32_e64 v92, v93, v85, s[0:1]
	v_cndmask_b32_e64 v85, v85, v93, s[0:1]
	v_cndmask_b32_e64 v93, v94, v86, s[0:1]
	v_cndmask_b32_e64 v86, v86, v94, s[0:1]
	v_cndmask_b32_e64 v94, v95, v87, s[0:1]
	v_cndmask_b32_e64 v87, v87, v95, s[0:1]
	v_cndmask_b32_e64 v95, v96, v88, s[0:1]
	v_cndmask_b32_e64 v88, v88, v96, s[0:1]
	v_cndmask_b32_e64 v96, v97, v89, s[0:1]
	v_cndmask_b32_e64 v89, v89, v97, s[0:1]
	v_cndmask_b32_e64 v97, v83, v90, s[0:1]
	v_cndmask_b32_e64 v83, v90, v83, s[0:1]
	ds_bpermute_b32 v69, v190, v69
	ds_bpermute_b32 v84, v190, v84
	ds_bpermute_b32 v85, v190, v85
	ds_bpermute_b32 v86, v190, v86
	ds_bpermute_b32 v87, v190, v87
	ds_bpermute_b32 v88, v190, v88
	ds_bpermute_b32 v89, v190, v89
	ds_bpermute_b32 v83, v190, v83
	s_waitcnt lgkmcnt(7)
	v_add_f32_e32 v69, v98, v69
	s_waitcnt lgkmcnt(6)
	v_add_f32_e32 v84, v91, v84
	s_waitcnt lgkmcnt(5)
	v_add_f32_e32 v85, v92, v85
	s_waitcnt lgkmcnt(4)
	v_add_f32_e32 v86, v93, v86
	s_waitcnt lgkmcnt(3)
	v_add_f32_e32 v87, v94, v87
	s_waitcnt lgkmcnt(2)
	v_add_f32_e32 v88, v95, v88
	s_waitcnt lgkmcnt(1)
	v_add_f32_e32 v89, v96, v89
	s_waitcnt lgkmcnt(0)
	v_add_f32_e32 v83, v97, v83
	v_cndmask_b32_e64 v90, v87, v69, s[2:3]
	v_cndmask_b32_e64 v69, v69, v87, s[2:3]
	v_cndmask_b32_e64 v87, v88, v84, s[2:3]
	v_cndmask_b32_e64 v84, v84, v88, s[2:3]
	v_cndmask_b32_e64 v88, v89, v85, s[2:3]
	v_cndmask_b32_e64 v85, v85, v89, s[2:3]
	v_cndmask_b32_e64 v89, v83, v86, s[2:3]
	v_cndmask_b32_e64 v83, v86, v83, s[2:3]
	ds_bpermute_b32 v69, v189, v69
	ds_bpermute_b32 v84, v189, v84
	ds_bpermute_b32 v85, v189, v85
	ds_bpermute_b32 v83, v189, v83
	s_add_i32 s57, s57, 16
	s_waitcnt lgkmcnt(3)
	v_add_f32_e32 v69, v90, v69
	s_waitcnt lgkmcnt(2)
	v_add_f32_e32 v84, v87, v84
	s_waitcnt lgkmcnt(1)
	v_add_f32_e32 v85, v88, v85
	s_waitcnt lgkmcnt(0)
	v_add_f32_e32 v83, v89, v83
	v_cndmask_b32_e64 v86, v85, v69, s[4:5]
	v_cndmask_b32_e64 v69, v69, v85, s[4:5]
	v_cndmask_b32_e64 v85, v83, v84, s[4:5]
	v_cndmask_b32_e64 v83, v84, v83, s[4:5]
	ds_bpermute_b32 v69, v188, v69
	ds_bpermute_b32 v83, v188, v83
	s_waitcnt lgkmcnt(1)
	v_add_f32_e32 v69, v86, v69
	s_waitcnt lgkmcnt(0)
	v_add_f32_e32 v83, v85, v83
	v_cndmask_b32_e64 v84, v83, v69, s[6:7]
	v_cndmask_b32_e64 v69, v69, v83, s[6:7]
	ds_bpermute_b32 v69, v163, v69
	s_waitcnt lgkmcnt(0)
	v_add_f32_e32 v69, v84, v69
	v_mov_b32_e32 v83, v69
	s_nop 1
	v_permlane16_swap_b32_e32 v69, v83
	v_add_f32_e32 v69, v69, v83
	v_mov_b32_e32 v83, v69
	s_nop 1
	v_permlane32_swap_b32_e32 v69, v83
	v_add_f32_e32 v69, v69, v83
	v_mul_f32_e32 v69, v66, v69
	v_fma_f32 v83, |v69|, s66, 1.0
	v_rcp_f32_e32 v83, v83
	v_mul_f32_e32 v84, v69, v69
	v_mul_f32_e32 v84, 0xbf38aa3b, v84
	v_exp_f32_e32 v84, v84
	v_fmamk_f32 v85, v83, 0x3f07dc22, v207
	v_fmaak_f32 v85, v83, v85, 0x3f35f0e3
	v_fmaak_f32 v85, v83, v85, 0xbe11a98e
	v_fmaak_f32 v85, v83, v85, 0x3e027906
	v_mul_f32_e32 v83, v83, v85
	v_mul_f32_e32 v83, v84, v83
	v_mul_f32_e32 v84, v69, v83
	v_fma_f32 v83, -v69, v83, v69
	v_cmp_gt_f32_e32 vcc, 0, v69
	s_nop 1
	v_cndmask_b32_e32 v69, v83, v84, vcc
	v_mul_f32_e32 v69, 0x3d4ccccd, v69
	v_mul_f32_e32 v69, v82, v69
	v_cmp_eq_u32_e32 vcc, s56, v193
	s_add_i32 s56, s56, 1
	s_cmpk_eq_i32 s57, 0x5f
	v_cndmask_b32_e32 v81, v81, v69, vcc
	s_cbranch_scc0 .LBB0_1419
	s_mov_b32 s56, 0
	v_mov_b32_e32 v82, 0
	s_movk_i32 s57, 0x5f
	s_cmp_eq_u32 s101, 0
	s_cbranch_scc1 .Lnb_1421
	s_barrier
.Lnb_1421:
.LBB0_1421:
	v_mov_b32_e32 v69, v1
	v_mov_b32_e32 v83, v1
	s_waitcnt vmcnt(9)
	v_dot8c_i32_i4_e32 v69, v6, v74
	v_dot8c_i32_i4_e32 v83, v6, v70
	v_dot8c_i32_i4_e32 v69, v7, v75
	v_dot8c_i32_i4_e32 v83, v7, v71
	v_dot8c_i32_i4_e32 v69, v8, v76
	v_dot8c_i32_i4_e32 v83, v8, v72
	s_add_i32 s62, s57, -15
	v_dot8c_i32_i4_e32 v69, v9, v77
	v_dot8c_i32_i4_e32 v83, v9, v73
	s_bitcmp0_b32 s62, 6
	s_cselect_b64 vcc, -1, 0
	s_nop 0
	v_lshl_add_u32 v6, v69, 4, v83
	v_cvt_f32_i32_e32 v69, v6
	v_cndmask_b32_e32 v6, v79, v78, vcc
	s_nop 0
	v_readlane_b32 s62, v6, s62
	s_lshl_b32 s63, s62, 10
	s_cmp_gt_u32 s56, 2
	s_cselect_b32 s62, 0x1000000, 0
	s_add_i32 s63, s63, s62
	buffer_load_dwordx4 v[6:9], v0, s[92:95], s63 offen
	v_mov_b32_e32 v83, v1
	v_mov_b32_e32 v84, v1
	s_waitcnt vmcnt(9)
	v_dot8c_i32_i4_e32 v83, v14, v74
	v_dot8c_i32_i4_e32 v84, v14, v70
	v_dot8c_i32_i4_e32 v83, v15, v75
	v_dot8c_i32_i4_e32 v84, v15, v71
	v_dot8c_i32_i4_e32 v83, v16, v76
	v_dot8c_i32_i4_e32 v84, v16, v72
	s_add_i32 s63, s57, -14
	v_dot8c_i32_i4_e32 v83, v17, v77
	v_dot8c_i32_i4_e32 v84, v17, v73
	s_bitcmp0_b32 s63, 6
	s_cselect_b64 vcc, -1, 0
	s_nop 0
	v_lshl_add_u32 v14, v83, 4, v84
	v_cvt_f32_i32_e32 v83, v14
	v_cndmask_b32_e32 v14, v79, v78, vcc
	s_nop 0
	v_readlane_b32 s63, v14, s63
	s_lshl_b32 s63, s63, 10
	s_add_i32 s63, s63, s62
	s_nop 2
	buffer_load_dwordx4 v[14:17], v0, s[92:95], s63 offen
	v_mov_b32_e32 v84, v1
	v_mov_b32_e32 v85, v1
	s_waitcnt vmcnt(9)
	v_dot8c_i32_i4_e32 v84, v30, v74
	v_dot8c_i32_i4_e32 v85, v30, v70
	v_dot8c_i32_i4_e32 v84, v31, v75
	v_dot8c_i32_i4_e32 v85, v31, v71
	v_dot8c_i32_i4_e32 v84, v32, v76
	v_dot8c_i32_i4_e32 v85, v32, v72
	s_add_i32 s63, s57, -13
	v_dot8c_i32_i4_e32 v84, v33, v77
	v_dot8c_i32_i4_e32 v85, v33, v73
	s_bitcmp0_b32 s63, 6
	s_cselect_b64 vcc, -1, 0
	s_nop 0
	v_lshl_add_u32 v30, v84, 4, v85
	v_cvt_f32_i32_e32 v84, v30
	v_cndmask_b32_e32 v30, v79, v78, vcc
	s_nop 0
	v_readlane_b32 s63, v30, s63
	s_lshl_b32 s63, s63, 10
	s_add_i32 s63, s63, s62
	s_nop 2
	buffer_load_dwordx4 v[30:33], v0, s[92:95], s63 offen
	v_mov_b32_e32 v85, v1
	v_mov_b32_e32 v86, v1
	s_waitcnt vmcnt(9)
	v_dot8c_i32_i4_e32 v85, v46, v74
	v_dot8c_i32_i4_e32 v86, v46, v70
	v_dot8c_i32_i4_e32 v85, v47, v75
	v_dot8c_i32_i4_e32 v86, v47, v71
	v_dot8c_i32_i4_e32 v85, v48, v76
	v_dot8c_i32_i4_e32 v86, v48, v72
	s_add_i32 s63, s57, -12
	v_dot8c_i32_i4_e32 v85, v49, v77
	v_dot8c_i32_i4_e32 v86, v49, v73
	s_bitcmp0_b32 s63, 6
	s_cselect_b64 vcc, -1, 0
	s_nop 0
	v_lshl_add_u32 v46, v85, 4, v86
	v_cvt_f32_i32_e32 v85, v46
	v_cndmask_b32_e32 v46, v79, v78, vcc
	s_nop 0
	v_readlane_b32 s63, v46, s63
	s_lshl_b32 s63, s63, 10
	s_add_i32 s63, s63, s62
	s_nop 2
	buffer_load_dwordx4 v[46:49], v0, s[92:95], s63 offen
	v_mov_b32_e32 v86, v1
	v_mov_b32_e32 v87, v1
	s_waitcnt vmcnt(9)
	v_dot8c_i32_i4_e32 v86, v2, v74
	v_dot8c_i32_i4_e32 v87, v2, v70
	v_dot8c_i32_i4_e32 v86, v3, v75
	v_dot8c_i32_i4_e32 v87, v3, v71
	v_dot8c_i32_i4_e32 v86, v4, v76
	v_dot8c_i32_i4_e32 v87, v4, v72
	s_add_i32 s63, s57, -11
	v_dot8c_i32_i4_e32 v86, v5, v77
	v_dot8c_i32_i4_e32 v87, v5, v73
	s_bitcmp0_b32 s63, 6
	s_cselect_b64 vcc, -1, 0
	s_nop 0
	v_lshl_add_u32 v2, v86, 4, v87
	v_cvt_f32_i32_e32 v86, v2
	v_cndmask_b32_e32 v2, v79, v78, vcc
	s_nop 0
	v_readlane_b32 s63, v2, s63
	s_lshl_b32 s63, s63, 10
	s_add_i32 s63, s63, s62
	s_nop 2
	buffer_load_dwordx4 v[2:5], v0, s[92:95], s63 offen
	v_mov_b32_e32 v87, v1
	v_mov_b32_e32 v88, v1
	s_waitcnt vmcnt(9)
	v_dot8c_i32_i4_e32 v87, v22, v74
	v_dot8c_i32_i4_e32 v88, v22, v70
	v_dot8c_i32_i4_e32 v87, v23, v75
	v_dot8c_i32_i4_e32 v88, v23, v71
	v_dot8c_i32_i4_e32 v87, v24, v76
	v_dot8c_i32_i4_e32 v88, v24, v72
	s_add_i32 s63, s57, -10
	v_dot8c_i32_i4_e32 v87, v25, v77
	v_dot8c_i32_i4_e32 v88, v25, v73
	s_bitcmp0_b32 s63, 6
	s_cselect_b64 vcc, -1, 0
	s_nop 0
	v_lshl_add_u32 v22, v87, 4, v88
	v_cvt_f32_i32_e32 v87, v22
	v_cndmask_b32_e32 v22, v79, v78, vcc
	s_nop 0
	v_readlane_b32 s63, v22, s63
	s_lshl_b32 s63, s63, 10
	s_add_i32 s63, s63, s62
	s_nop 2
	buffer_load_dwordx4 v[22:25], v0, s[92:95], s63 offen
	v_mov_b32_e32 v88, v1
	v_mov_b32_e32 v89, v1
	s_waitcnt vmcnt(9)
	v_dot8c_i32_i4_e32 v88, v38, v74
	v_dot8c_i32_i4_e32 v89, v38, v70
	v_dot8c_i32_i4_e32 v88, v39, v75
	v_dot8c_i32_i4_e32 v89, v39, v71
	v_dot8c_i32_i4_e32 v88, v40, v76
	v_dot8c_i32_i4_e32 v89, v40, v72
	s_add_i32 s63, s57, -9
	v_dot8c_i32_i4_e32 v88, v41, v77
	v_dot8c_i32_i4_e32 v89, v41, v73
	s_bitcmp0_b32 s63, 6
	s_cselect_b64 vcc, -1, 0
	s_nop 0
	v_lshl_add_u32 v38, v88, 4, v89
	v_cvt_f32_i32_e32 v88, v38
	v_cndmask_b32_e32 v38, v79, v78, vcc
	s_nop 0
	v_readlane_b32 s63, v38, s63
	s_lshl_b32 s63, s63, 10
	s_add_i32 s63, s63, s62
	s_nop 2
	buffer_load_dwordx4 v[38:41], v0, s[92:95], s63 offen
	v_mov_b32_e32 v89, v1
	v_mov_b32_e32 v90, v1
	s_waitcnt vmcnt(9)
	v_dot8c_i32_i4_e32 v89, v54, v74
	v_dot8c_i32_i4_e32 v90, v54, v70
	v_dot8c_i32_i4_e32 v89, v55, v75
	v_dot8c_i32_i4_e32 v90, v55, v71
	v_dot8c_i32_i4_e32 v89, v56, v76
	v_dot8c_i32_i4_e32 v90, v56, v72
	s_add_i32 s63, s57, -8
	v_dot8c_i32_i4_e32 v89, v57, v77
	v_dot8c_i32_i4_e32 v90, v57, v73
	s_bitcmp0_b32 s63, 6
	s_cselect_b64 vcc, -1, 0
	s_nop 0
	v_lshl_add_u32 v54, v89, 4, v90
	v_cvt_f32_i32_e32 v89, v54
	v_cndmask_b32_e32 v54, v79, v78, vcc
	s_nop 0
	v_readlane_b32 s63, v54, s63
	s_lshl_b32 s63, s63, 10
	s_add_i32 s63, s63, s62
	s_nop 2
	buffer_load_dwordx4 v[54:57], v0, s[92:95], s63 offen
	v_mov_b32_e32 v90, v1
	v_mov_b32_e32 v91, v1
	s_waitcnt vmcnt(9)
	v_dot8c_i32_i4_e32 v90, v10, v74
	v_dot8c_i32_i4_e32 v91, v10, v70
	v_dot8c_i32_i4_e32 v90, v11, v75
	v_dot8c_i32_i4_e32 v91, v11, v71
	v_dot8c_i32_i4_e32 v90, v12, v76
	v_dot8c_i32_i4_e32 v91, v12, v72
	s_add_i32 s63, s57, -7
	v_dot8c_i32_i4_e32 v90, v13, v77
	v_dot8c_i32_i4_e32 v91, v13, v73
	s_bitcmp0_b32 s63, 6
	s_cselect_b64 vcc, -1, 0
	s_nop 0
	v_lshl_add_u32 v10, v90, 4, v91
	v_cvt_f32_i32_e32 v90, v10
	v_cndmask_b32_e32 v10, v79, v78, vcc
	s_nop 0
	v_readlane_b32 s63, v10, s63
	s_lshl_b32 s63, s63, 10
	s_add_i32 s63, s63, s62
	s_nop 2
	buffer_load_dwordx4 v[10:13], v0, s[92:95], s63 offen
	v_mov_b32_e32 v91, v1
	v_mov_b32_e32 v92, v1
	s_waitcnt vmcnt(9)
	v_dot8c_i32_i4_e32 v91, v26, v74
	v_dot8c_i32_i4_e32 v92, v26, v70
	v_dot8c_i32_i4_e32 v91, v27, v75
	v_dot8c_i32_i4_e32 v92, v27, v71
	v_dot8c_i32_i4_e32 v91, v28, v76
	v_dot8c_i32_i4_e32 v92, v28, v72
	s_add_i32 s63, s57, -6
	v_dot8c_i32_i4_e32 v91, v29, v77
	v_dot8c_i32_i4_e32 v92, v29, v73
	s_bitcmp0_b32 s63, 6
	s_cselect_b64 vcc, -1, 0
	s_nop 0
	v_lshl_add_u32 v26, v91, 4, v92
	v_cvt_f32_i32_e32 v91, v26
	v_cndmask_b32_e32 v26, v79, v78, vcc
	s_nop 0
	v_readlane_b32 s63, v26, s63
	s_lshl_b32 s63, s63, 10
	s_add_i32 s63, s63, s62
	s_nop 2
	buffer_load_dwordx4 v[26:29], v0, s[92:95], s63 offen
	v_mov_b32_e32 v92, v1
	v_mov_b32_e32 v93, v1
	s_waitcnt vmcnt(9)
	v_dot8c_i32_i4_e32 v92, v42, v74
	v_dot8c_i32_i4_e32 v93, v42, v70
	v_dot8c_i32_i4_e32 v92, v43, v75
	v_dot8c_i32_i4_e32 v93, v43, v71
	v_dot8c_i32_i4_e32 v92, v44, v76
	v_dot8c_i32_i4_e32 v93, v44, v72
	s_add_i32 s63, s57, -5
	v_dot8c_i32_i4_e32 v92, v45, v77
	v_dot8c_i32_i4_e32 v93, v45, v73
	s_bitcmp0_b32 s63, 6
	s_cselect_b64 vcc, -1, 0
	s_nop 0
	v_lshl_add_u32 v42, v92, 4, v93
	v_cvt_f32_i32_e32 v92, v42
	v_cndmask_b32_e32 v42, v79, v78, vcc
	s_nop 0
	v_readlane_b32 s63, v42, s63
	s_lshl_b32 s63, s63, 10
	s_add_i32 s63, s63, s62
	s_nop 2
	buffer_load_dwordx4 v[42:45], v0, s[92:95], s63 offen
	v_mov_b32_e32 v93, v1
	v_mov_b32_e32 v94, v1
	s_waitcnt vmcnt(9)
	v_dot8c_i32_i4_e32 v93, v58, v74
	v_dot8c_i32_i4_e32 v94, v58, v70
	v_dot8c_i32_i4_e32 v93, v59, v75
	v_dot8c_i32_i4_e32 v94, v59, v71
	v_dot8c_i32_i4_e32 v93, v60, v76
	v_dot8c_i32_i4_e32 v94, v60, v72
	s_add_i32 s63, s57, -4
	v_dot8c_i32_i4_e32 v93, v61, v77
	v_dot8c_i32_i4_e32 v94, v61, v73
	s_bitcmp0_b32 s63, 6
	s_cselect_b64 vcc, -1, 0
	s_nop 0
	v_lshl_add_u32 v58, v93, 4, v94
	v_cvt_f32_i32_e32 v93, v58
	v_cndmask_b32_e32 v58, v79, v78, vcc
	s_nop 0
	v_readlane_b32 s63, v58, s63
	s_lshl_b32 s63, s63, 10
	s_add_i32 s63, s63, s62
	s_nop 2
	buffer_load_dwordx4 v[58:61], v0, s[92:95], s63 offen
	v_mov_b32_e32 v94, v1
	v_mov_b32_e32 v95, v1
	s_waitcnt vmcnt(9)
	v_dot8c_i32_i4_e32 v94, v18, v74
	v_dot8c_i32_i4_e32 v95, v18, v70
	v_dot8c_i32_i4_e32 v94, v19, v75
	v_dot8c_i32_i4_e32 v95, v19, v71
	v_dot8c_i32_i4_e32 v94, v20, v76
	v_dot8c_i32_i4_e32 v95, v20, v72
	s_add_i32 s63, s57, -3
	v_dot8c_i32_i4_e32 v94, v21, v77
	v_dot8c_i32_i4_e32 v95, v21, v73
	s_bitcmp0_b32 s63, 6
	s_cselect_b64 vcc, -1, 0
	s_nop 0
	v_lshl_add_u32 v18, v94, 4, v95
	v_cvt_f32_i32_e32 v94, v18
	v_cndmask_b32_e32 v18, v79, v78, vcc
	s_nop 0
	v_readlane_b32 s63, v18, s63
	s_lshl_b32 s63, s63, 10
	s_add_i32 s63, s63, s62
	s_nop 2
	buffer_load_dwordx4 v[18:21], v0, s[92:95], s63 offen
	v_mov_b32_e32 v95, v1
	v_mov_b32_e32 v96, v1
	s_waitcnt vmcnt(9)
	v_dot8c_i32_i4_e32 v95, v34, v74
	v_dot8c_i32_i4_e32 v96, v34, v70
	v_dot8c_i32_i4_e32 v95, v35, v75
	v_dot8c_i32_i4_e32 v96, v35, v71
	v_dot8c_i32_i4_e32 v95, v36, v76
	v_dot8c_i32_i4_e32 v96, v36, v72
	s_add_i32 s63, s57, -2
	v_dot8c_i32_i4_e32 v95, v37, v77
	v_dot8c_i32_i4_e32 v96, v37, v73
	s_bitcmp0_b32 s63, 6
	s_cselect_b64 vcc, -1, 0
	s_nop 0
	v_lshl_add_u32 v34, v95, 4, v96
	v_cvt_f32_i32_e32 v95, v34
	v_cndmask_b32_e32 v34, v79, v78, vcc
	s_nop 0
	v_readlane_b32 s63, v34, s63
	s_lshl_b32 s63, s63, 10
	s_add_i32 s63, s63, s62
	s_nop 2
	buffer_load_dwordx4 v[34:37], v0, s[92:95], s63 offen
	v_mov_b32_e32 v96, v1
	v_mov_b32_e32 v97, v1
	s_waitcnt vmcnt(9)
	v_dot8c_i32_i4_e32 v96, v50, v74
	v_dot8c_i32_i4_e32 v97, v50, v70
	v_dot8c_i32_i4_e32 v96, v51, v75
	v_dot8c_i32_i4_e32 v97, v51, v71
	v_dot8c_i32_i4_e32 v96, v52, v76
	v_dot8c_i32_i4_e32 v97, v52, v72
	s_add_i32 s63, s57, -1
	v_dot8c_i32_i4_e32 v96, v53, v77
	v_dot8c_i32_i4_e32 v97, v53, v73
	s_bitcmp0_b32 s63, 6
	s_cselect_b64 vcc, -1, 0
	s_nop 0
	v_lshl_add_u32 v50, v96, 4, v97
	v_cvt_f32_i32_e32 v96, v50
	v_cndmask_b32_e32 v50, v79, v78, vcc
	s_nop 0
	v_readlane_b32 s63, v50, s63
	s_lshl_b32 s63, s63, 10
	s_add_i32 s63, s63, s62
	s_nop 2
	buffer_load_dwordx4 v[50:53], v0, s[92:95], s63 offen
	v_mov_b32_e32 v97, v1
	v_mov_b32_e32 v98, v1
	s_waitcnt vmcnt(9)
	v_dot8c_i32_i4_e32 v97, v62, v74
	v_dot8c_i32_i4_e32 v98, v62, v70
	v_dot8c_i32_i4_e32 v97, v63, v75
	v_dot8c_i32_i4_e32 v98, v63, v71
	v_dot8c_i32_i4_e32 v97, v64, v76
	v_dot8c_i32_i4_e32 v98, v64, v72
	v_dot8c_i32_i4_e32 v97, v65, v77
	v_dot8c_i32_i4_e32 v98, v65, v73
	s_bitcmp0_b32 s57, 6
	s_cselect_b64 vcc, -1, 0
	s_nop 0
	v_lshl_add_u32 v62, v97, 4, v98
	v_cvt_f32_i32_e32 v97, v62
	v_cndmask_b32_e32 v62, v79, v78, vcc
	s_nop 0
	v_readlane_b32 s63, v62, s57
	s_lshl_b32 s63, s63, 10
	s_add_i32 s63, s63, s62
	s_nop 2
	buffer_load_dwordx4 v[62:65], v0, s[92:95], s63 offen
	v_cndmask_b32_e64 v98, v90, v69, s[0:1]
	v_cndmask_b32_e64 v69, v69, v90, s[0:1]
	v_cndmask_b32_e64 v90, v91, v83, s[0:1]
	v_cndmask_b32_e64 v83, v83, v91, s[0:1]
	v_cndmask_b32_e64 v91, v92, v84, s[0:1]
	v_cndmask_b32_e64 v84, v84, v92, s[0:1]
	v_cndmask_b32_e64 v92, v93, v85, s[0:1]
	v_cndmask_b32_e64 v85, v85, v93, s[0:1]
	v_cndmask_b32_e64 v93, v94, v86, s[0:1]
	v_cndmask_b32_e64 v86, v86, v94, s[0:1]
	v_cndmask_b32_e64 v94, v95, v87, s[0:1]
	v_cndmask_b32_e64 v87, v87, v95, s[0:1]
	v_cndmask_b32_e64 v95, v96, v88, s[0:1]
	v_cndmask_b32_e64 v88, v88, v96, s[0:1]
	v_cndmask_b32_e64 v96, v97, v89, s[0:1]
	v_cndmask_b32_e64 v89, v89, v97, s[0:1]
	ds_bpermute_b32 v69, v190, v69
	ds_bpermute_b32 v83, v190, v83
	ds_bpermute_b32 v84, v190, v84
	ds_bpermute_b32 v85, v190, v85
	ds_bpermute_b32 v86, v190, v86
	ds_bpermute_b32 v87, v190, v87
	ds_bpermute_b32 v88, v190, v88
	ds_bpermute_b32 v89, v190, v89
	s_waitcnt lgkmcnt(7)
; __device__ __forceinline__ int shl_i(int v, int from_lane) { return __builtin_amdgcn_ds_bpermute(from_lane << 2, v); }
;     ...
;         const float wm = wave_max(fmaxf(fabsf(w0), fabsf(w1)));
;         const float wsq = (wm > 0.f) ? 127.0f / wm : 0.f;
;         const int q0 = (int)rintf(w0 * wsq), q1 = (int)rintf(w1 * wsq);
;         const int c8 = 8 * (int)wave_sum((float)(q0 + q1));
;         const int pk0 = (q0 & 0xFF) | ((shl_i(q0, lane + 1) & 0xFF) << 8) | ((shl_i(q0, lane + 2) & 0xFF) << 16) | (shl_i(q0, lane + 3) << 24);
;         const int pk1 = (q1 & 0xFF) | ((shl_i(q1, lane + 1) & 0xFF) << 8) | ((shl_i(q1, lane + 2) & 0xFF) << 16) | (shl_i(q1, lane + 3) << 24);
;         int acci[32];
; #pragma unroll
;         for (int i = 0; i < 32; ++i) acci[i] = 0;
	v_add_f32_e32 v69, v98, v69
	s_waitcnt lgkmcnt(6)
	v_add_f32_e32 v83, v90, v83
	s_waitcnt lgkmcnt(5)
	v_add_f32_e32 v84, v91, v84
	s_waitcnt lgkmcnt(4)
	v_add_f32_e32 v85, v92, v85
	s_waitcnt lgkmcnt(3)
	v_add_f32_e32 v86, v93, v86
	s_waitcnt lgkmcnt(2)
	v_add_f32_e32 v87, v94, v87
	s_waitcnt lgkmcnt(1)
	v_add_f32_e32 v88, v95, v88
	s_waitcnt lgkmcnt(0)
	v_add_f32_e32 v89, v96, v89
	v_cndmask_b32_e64 v90, v86, v69, s[2:3]
	v_cndmask_b32_e64 v69, v69, v86, s[2:3]
	v_cndmask_b32_e64 v86, v87, v83, s[2:3]
	v_cndmask_b32_e64 v83, v83, v87, s[2:3]
	v_cndmask_b32_e64 v87, v88, v84, s[2:3]
	v_cndmask_b32_e64 v84, v84, v88, s[2:3]
	v_cndmask_b32_e64 v88, v89, v85, s[2:3]
	v_cndmask_b32_e64 v85, v85, v89, s[2:3]
	ds_bpermute_b32 v69, v189, v69
	ds_bpermute_b32 v83, v189, v83
	ds_bpermute_b32 v84, v189, v84
	ds_bpermute_b32 v85, v189, v85
	s_add_i32 s57, s57, 16
	s_waitcnt lgkmcnt(3)
	v_add_f32_e32 v69, v90, v69
	s_waitcnt lgkmcnt(2)
	v_add_f32_e32 v83, v86, v83
	s_waitcnt lgkmcnt(1)
	v_add_f32_e32 v84, v87, v84
	s_waitcnt lgkmcnt(0)
	v_add_f32_e32 v85, v88, v85
	v_cndmask_b32_e64 v86, v84, v69, s[4:5]
	v_cndmask_b32_e64 v69, v69, v84, s[4:5]
	v_cndmask_b32_e64 v84, v85, v83, s[4:5]
	v_cndmask_b32_e64 v83, v83, v85, s[4:5]
	ds_bpermute_b32 v69, v188, v69
	ds_bpermute_b32 v83, v188, v83
	s_waitcnt lgkmcnt(1)
	v_add_f32_e32 v69, v86, v69
	s_waitcnt lgkmcnt(0)
	v_add_f32_e32 v83, v84, v83
	v_cndmask_b32_e64 v84, v83, v69, s[6:7]
	v_cndmask_b32_e64 v69, v69, v83, s[6:7]
	ds_bpermute_b32 v69, v163, v69
	s_waitcnt lgkmcnt(0)
	v_add_f32_e32 v69, v84, v69
	v_mov_b32_e32 v83, v69
	s_nop 1
	v_permlane16_swap_b32_e32 v69, v83
	v_add_f32_e32 v69, v69, v83
	v_mov_b32_e32 v83, v69
	s_nop 1
	v_permlane32_swap_b32_e32 v69, v83
	v_add_f32_e32 v69, v69, v83
	v_mul_f32_e32 v69, v66, v69
	v_fma_f32 v83, |v69|, s66, 1.0
	v_rcp_f32_e32 v83, v83
	v_mul_f32_e32 v84, v69, v69
	v_mul_f32_e32 v84, 0xbf38aa3b, v84
	v_exp_f32_e32 v84, v84
	v_fmamk_f32 v85, v83, 0x3f07dc22, v207
	v_fmaak_f32 v85, v83, v85, 0x3f35f0e3
	v_fmaak_f32 v85, v83, v85, 0xbe11a98e
	v_fmaak_f32 v85, v83, v85, 0x3e027906
	v_mul_f32_e32 v83, v83, v85
	v_mul_f32_e32 v83, v84, v83
	v_mul_f32_e32 v84, v69, v83
	v_fma_f32 v83, -v69, v83, v69
	v_cmp_gt_f32_e32 vcc, 0, v69
	s_nop 1
	v_cndmask_b32_e32 v69, v83, v84, vcc
	v_mul_f32_e32 v69, 0x3d4ccccd, v69
	v_mul_f32_e32 v69, v80, v69
	v_cmp_eq_u32_e32 vcc, s56, v193
	s_add_i32 s56, s56, 1
	s_cmpk_eq_i32 s57, 0x9f
	v_cndmask_b32_e32 v82, v82, v69, vcc
	s_cbranch_scc0 .LBB0_1421
	v_max_f32_e64 v66, |v82|, |v82|
	v_max_f32_e64 v69, |v81|, |v81|
	v_max_f32_e32 v66, v69, v66
	v_mov_b32_e32 v69, 0
	s_mov_b32 s57, 0x42fe0000
	v_mbcnt_lo_u32_b32 v69, -1, v69
	v_mbcnt_hi_u32_b32 v69, -1, v69
	v_lshlrev_b32_e32 v71, 2, v69
	v_xor_b32_e32 v69, 0x80, v71
	ds_bpermute_b32 v69, v69, v66
	v_xor_b32_e32 v70, 64, v71
	v_xor_b32_e32 v72, 8, v71
	v_mov_b32_e32 v83, 0
	s_waitcnt lgkmcnt(0)
	v_max_f32_e32 v69, v69, v69
	v_max_f32_e32 v66, v66, v69
	ds_bpermute_b32 v69, v70, v66
	v_xor_b32_e32 v70, 32, v71
	s_movk_i32 s56, 0x9f
	v_mov_b32_e32 v74, 0
	v_mov_b32_e32 v75, 0
	s_waitcnt lgkmcnt(0)
	v_max_f32_e32 v69, v69, v69
	v_max_f32_e32 v66, v66, v69
	ds_bpermute_b32 v69, v70, v66
	v_xor_b32_e32 v70, 16, v71
	v_xor_b32_e32 v71, 4, v71
	v_mov_b32_e32 v76, 0
	v_mov_b32_e32 v80, 0
	s_waitcnt lgkmcnt(0)
	v_max_f32_e32 v69, v69, v69
	v_max_f32_e32 v69, v66, v69
	ds_bpermute_b32 v70, v70, v69
	v_mov_b32_e32 v66, 0
	v_mov_b32_e32 v94, 0
	v_mov_b32_e32 v95, 0
	v_mov_b32_e32 v96, 0
	s_waitcnt lgkmcnt(0)
	v_max_f32_e32 v70, v70, v70
	v_max_f32_e32 v73, v69, v70
	ds_bpermute_b32 v72, v72, v73
	v_mov_b32_e32 v69, 0
	v_mov_b32_e32 v70, 0
	v_mov_b32_e32 v97, 0
	v_mov_b32_e32 v98, 0
	s_waitcnt lgkmcnt(0)
	v_max_f32_e32 v72, v72, v72
	v_max_f32_e32 v77, v73, v72
	ds_bpermute_b32 v71, v71, v77
	v_mov_b32_e32 v72, 0
	v_mov_b32_e32 v73, 0
	v_mov_b32_e32 v99, 0
	v_mov_b32_e32 v100, 0
	s_waitcnt lgkmcnt(0)
	v_max_f32_e32 v71, v71, v71
	v_max_f32_e32 v71, v77, v71
	v_div_scale_f32 v77, s[62:63], v71, v71, s57
	v_rcp_f32_e32 v84, v77
	v_div_scale_f32 v85, vcc, s57, v71, s57
	v_mov_b32_e32 v101, 0
	v_fma_f32 v86, -v77, v84, 1.0
	v_fmac_f32_e32 v84, v86, v84
	v_mul_f32_e32 v86, v85, v84
	v_fma_f32 v87, -v77, v86, v85
	v_fmac_f32_e32 v86, v87, v84
	v_fma_f32 v77, -v77, v86, v85
	v_div_fmas_f32 v77, v77, v84, v86
	v_div_fixup_f32 v77, v77, v71, s57
	v_cmp_lt_f32_e32 vcc, 0, v71
	s_mov_b32 s57, 0xc0c0500
	v_mov_b32_e32 v85, 0
	v_cndmask_b32_e32 v77, 0, v77, vcc
	v_mul_f32_e32 v81, v81, v77
	v_mul_f32_e32 v77, v82, v77
	v_rndne_f32_e32 v81, v81
	v_rndne_f32_e32 v77, v77
	v_cvt_i32_f32_e32 v82, v81
	v_cvt_i32_f32_e32 v107, v77
	v_mbcnt_lo_u32_b32 v81, -1, v83
	v_mbcnt_hi_u32_b32 v81, -1, v81
	v_lshlrev_b32_e32 v84, 2, v81
	v_add_u32_e32 v83, v82, v107
	v_cvt_f32_i32_e32 v83, v83
	v_xor_b32_e32 v81, 0x80, v84
	v_xor_b32_e32 v88, 64, v84
	v_xor_b32_e32 v89, 16, v84
	ds_bpermute_b32 v87, v81, v83
	v_xor_b32_e32 v90, 8, v84
	ds_bpermute_b32 v91, v195, v82
	ds_bpermute_b32 v92, v196, v82
	ds_bpermute_b32 v108, v194, v107
	s_waitcnt lgkmcnt(3)
	v_add_f32_e32 v83, v87, v83
	ds_bpermute_b32 v87, v88, v83
	v_xor_b32_e32 v88, 32, v84
	v_xor_b32_e32 v84, 4, v84
	ds_bpermute_b32 v109, v195, v107
	ds_bpermute_b32 v110, v196, v107
	s_waitcnt lgkmcnt(2)
	v_add_f32_e32 v83, v83, v87
	ds_bpermute_b32 v87, v88, v83
	ds_bpermute_b32 v88, v194, v82
	v_mov_b32_e32 v77, 0
	v_mov_b32_e32 v81, 0
	v_mov_b32_e32 v86, 0
	s_waitcnt lgkmcnt(1)
	v_add_f32_e32 v83, v83, v87
	ds_bpermute_b32 v87, v89, v83
	s_waitcnt lgkmcnt(1)
	v_lshlrev_b32_e32 v88, 8, v88
	v_lshlrev_b32_e32 v89, 16, v91
	v_perm_b32 v82, v88, v82, s57
	v_and_b32_e32 v88, 0xff0000, v89
	s_waitcnt lgkmcnt(0)
	v_add_f32_e32 v83, v83, v87
	ds_bpermute_b32 v87, v90, v83
	v_lshlrev_b32_e32 v90, 24, v92
	v_or3_b32 v111, v82, v88, v90
	v_mov_b32_e32 v82, 0
	v_mov_b32_e32 v88, 0
	s_waitcnt lgkmcnt(0)
	v_add_f32_e32 v103, v83, v87
	ds_bpermute_b32 v104, v84, v103
	v_mov_b32_e32 v84, 0
	v_mov_b32_e32 v87, 0
	v_mov_b32_e32 v89, 0
	v_mov_b32_e32 v90, 0
	v_mov_b32_e32 v91, 0
	v_mov_b32_e32 v92, 0
	v_mov_b32_e32 v93, 0
	v_mov_b32_e32 v102, 0
	v_mov_b32_e32 v83, 0
	s_cmp_eq_u32 s101, 0
	s_cbranch_scc1 .Lnb_1423
	s_barrier
